# second half of the layer-0 relu/cvt/LDS-store work interleaved under the 16 MFMAs of the first own k-step
# speedup vs baseline: 1.0103x; 1.0103x over previous
.LBB1_4:
	s_and_saveexec_b64 s[8:9], s[2:3]
	v_perm_b32 v5, v1, v102, s23
	v_perm_b32 v9, v121, v103, s23
	v_perm_b32 v17, v144, v115, s23
	v_perm_b32 v29, v145, v116, s23
	s_or_b64 exec, exec, s[8:9]
	v_mfma_f32_16x16x32_f16 v[164:167], v[30:33], v[2:5], 0
	v_mfma_f32_16x16x32_f16 v[180:183], v[22:25], v[2:5], 0
	s_cmp_lg_u32 s22, 0x818000
	v_mfma_f32_16x16x32_f16 v[168:171], v[30:33], v[6:9], 0
	v_mfma_f32_16x16x32_f16 v[184:187], v[22:25], v[6:9], 0
	s_cselect_b32 s9, s11, 15
	v_mfma_f32_16x16x32_f16 v[172:175], v[30:33], v[14:17], 0
	v_mfma_f32_16x16x32_f16 v[188:191], v[22:25], v[14:17], 0
	v_mfma_f32_16x16x32_f16 v[176:179], v[30:33], v[26:29], 0
	v_mfma_f32_16x16x32_f16 v[192:195], v[22:25], v[26:29], 0
	v_mfma_f32_16x16x32_f16 v[208:211], v[18:21], v[2:5], 0
	v_cvt_pk_f16_f32 v122, v164, v165
	v_cvt_pk_f16_f32 v123, v166, v167
	v_pk_max_f16 v122, v122, 0
	v_pk_max_f16 v123, v123, 0
	v_cvt_pk_f16_f32 v124, v180, v181
	v_cvt_pk_f16_f32 v125, v182, v183
	v_pk_max_f16 v124, v124, 0
	v_pk_max_f16 v125, v125, 0
	ds_write_b128 v107, v[122:125]
	v_mfma_f32_16x16x32_f16 v[224:227], v[10:13], v[2:5], 0
	v_cvt_pk_f16_f32 v126, v168, v169
	v_cvt_pk_f16_f32 v127, v170, v171
	v_pk_max_f16 v126, v126, 0
	v_pk_max_f16 v127, v127, 0
	v_cvt_pk_f16_f32 v128, v184, v185
	v_cvt_pk_f16_f32 v129, v186, v187
	v_pk_max_f16 v128, v128, 0
	v_pk_max_f16 v129, v129, 0
	ds_write_b128 v107, v[126:129] offset:16384
	v_mfma_f32_16x16x32_f16 v[212:215], v[18:21], v[6:9], 0
	v_cvt_pk_f16_f32 v134, v172, v173
	v_cvt_pk_f16_f32 v135, v174, v175
	v_pk_max_f16 v134, v134, 0
	v_pk_max_f16 v135, v135, 0
	v_cvt_pk_f16_f32 v136, v188, v189
	v_cvt_pk_f16_f32 v137, v190, v191
	v_pk_max_f16 v136, v136, 0
	v_pk_max_f16 v137, v137, 0
	ds_write_b128 v107, v[134:137] offset:32768
	v_mfma_f32_16x16x32_f16 v[228:231], v[10:13], v[6:9], 0
	v_cvt_pk_f16_f32 v138, v176, v177
	v_cvt_pk_f16_f32 v139, v178, v179
	v_pk_max_f16 v138, v138, 0
	v_pk_max_f16 v139, v139, 0
	v_cvt_pk_f16_f32 v140, v192, v193
	v_cvt_pk_f16_f32 v141, v194, v195
	v_pk_max_f16 v140, v140, 0
	v_pk_max_f16 v141, v141, 0
	ds_write_b128 v107, v[138:141] offset:49152
	v_mfma_f32_16x16x32_f16 v[216:219], v[18:21], v[14:17], 0
	v_mfma_f32_16x16x32_f16 v[232:235], v[10:13], v[14:17], 0
	v_mfma_f32_16x16x32_f16 v[220:223], v[18:21], v[26:29], 0
	v_mfma_f32_16x16x32_f16 v[236:239], v[10:13], v[26:29], 0
	v_add_u32_e32 v111, s64, v111
	v_add_u32_e32 v98, s65, v98
	s_lshl_b32 s20, s9, 7
	v_lshl_add_u64 v[0:1], s[20:21], 3, v[132:133]
	s_add_i32 s25, s22, s34
	s_lshl_b32 s8, s9, 8
	buffer_load_dwordx4 v[192:195], v147, s[16:19], s25 offen
	buffer_load_dwordx4 v[196:199], v148, s[16:19], s25 offen
	buffer_load_dwordx4 v[200:203], v149, s[16:19], s25 offen
	buffer_load_dwordx4 v[204:207], v150, s[16:19], s25 offen
	s_waitcnt vmcnt(19)
	v_mfma_f32_16x16x32_f16 v[164:167], v[58:61], v[122:125], v[240:243]
	v_cvt_pk_f16_f32 v142, v208, v209
	v_cvt_pk_f16_f32 v143, v210, v211
	v_mfma_f32_16x16x32_f16 v[168:171], v[58:61], v[126:129], v[240:243]
	v_pk_max_f16 v142, v142, 0
	v_pk_max_f16 v143, v143, 0
	v_mfma_f32_16x16x32_f16 v[172:175], v[58:61], v[134:137], v[240:243]
	v_cvt_pk_f16_f32 v144, v224, v225
	v_cvt_pk_f16_f32 v145, v226, v227
	v_mfma_f32_16x16x32_f16 v[10:13], v[58:61], v[138:141], v[240:243]
	v_pk_max_f16 v144, v144, 0
	v_pk_max_f16 v145, v145, 0
	ds_write_b128 v108, v[142:145]
	s_waitcnt vmcnt(18)
	v_mfma_f32_16x16x32_f16 v[58:61], v[54:57], v[122:125], v[244:247]
	v_cvt_pk_f16_f32 v152, v212, v213
	v_cvt_pk_f16_f32 v153, v214, v215
	v_mfma_f32_16x16x32_f16 v[176:179], v[54:57], v[126:129], v[244:247]
	v_pk_max_f16 v152, v152, 0
	v_pk_max_f16 v153, v153, 0
	v_mfma_f32_16x16x32_f16 v[180:183], v[54:57], v[134:137], v[244:247]
	v_cvt_pk_f16_f32 v154, v228, v229
	v_cvt_pk_f16_f32 v155, v230, v231
	v_mfma_f32_16x16x32_f16 v[18:21], v[54:57], v[138:141], v[244:247]
	v_pk_max_f16 v154, v154, 0
	v_pk_max_f16 v155, v155, 0
	ds_write_b128 v108, v[152:155] offset:16384
	s_waitcnt vmcnt(17)
	v_mfma_f32_16x16x32_f16 v[54:57], v[50:53], v[122:125], v[248:251]
	v_cvt_pk_f16_f32 v156, v216, v217
	v_cvt_pk_f16_f32 v157, v218, v219
	v_mfma_f32_16x16x32_f16 v[184:187], v[50:53], v[126:129], v[248:251]
	v_pk_max_f16 v156, v156, 0
	v_pk_max_f16 v157, v157, 0
	v_mfma_f32_16x16x32_f16 v[188:191], v[50:53], v[134:137], v[248:251]
	v_cvt_pk_f16_f32 v158, v232, v233
	v_cvt_pk_f16_f32 v159, v234, v235
	v_mfma_f32_16x16x32_f16 v[22:25], v[50:53], v[138:141], v[248:251]
	v_pk_max_f16 v158, v158, 0
	v_pk_max_f16 v159, v159, 0
	ds_write_b128 v108, v[156:159] offset:32768
	s_waitcnt vmcnt(16)
	v_mfma_f32_16x16x32_f16 v[50:53], v[38:41], v[122:125], v[252:255]
	v_cvt_pk_f16_f32 v160, v220, v221
	v_cvt_pk_f16_f32 v161, v222, v223
	v_mfma_f32_16x16x32_f16 v[122:125], v[38:41], v[126:129], v[252:255]
	v_pk_max_f16 v160, v160, 0
	v_pk_max_f16 v161, v161, 0
	v_mfma_f32_16x16x32_f16 v[126:129], v[38:41], v[134:137], v[252:255]
	v_cvt_pk_f16_f32 v162, v236, v237
	v_cvt_pk_f16_f32 v163, v238, v239
	v_mfma_f32_16x16x32_f16 v[38:41], v[38:41], v[138:141], v[252:255]
	v_pk_max_f16 v162, v162, 0
	v_pk_max_f16 v163, v163, 0
	ds_write_b128 v108, v[160:163] offset:49152
	s_add_i32 s9, s22, s35
	s_waitcnt vmcnt(15)
	v_mfma_f32_16x16x32_f16 v[164:167], v[94:97], v[142:145], v[164:167]
	v_mfma_f32_16x16x32_f16 v[168:171], v[94:97], v[152:155], v[168:171]
	s_waitcnt vmcnt(14)
	v_mfma_f32_16x16x32_f16 v[58:61], v[90:93], v[142:145], v[58:61]
	v_mfma_f32_16x16x32_f16 v[176:179], v[90:93], v[152:155], v[176:179]
	s_waitcnt vmcnt(13)
	v_mfma_f32_16x16x32_f16 v[54:57], v[78:81], v[142:145], v[54:57]
	v_mfma_f32_16x16x32_f16 v[184:187], v[78:81], v[152:155], v[184:187]
	s_waitcnt vmcnt(12)
	v_mfma_f32_16x16x32_f16 v[50:53], v[34:37], v[142:145], v[50:53]
	buffer_load_dwordx4 v[140:143], v147, s[16:19], s9 offen
	buffer_load_dwordx4 v[220:223], v148, s[16:19], s9 offen
	v_mfma_f32_16x16x32_f16 v[122:125], v[34:37], v[152:155], v[122:125]
	buffer_load_dwordx4 v[152:155], v149, s[16:19], s9 offen
	buffer_load_dwordx4 v[224:227], v150, s[16:19], s9 offen
	s_mov_b32 s9, s21
	s_waitcnt lgkmcnt(0)
	s_barrier
	v_add_u32_e32 v99, s66, v99
	ds_read_b128 v[136:139], v99
	ds_read_b128 v[208:211], v99 offset:16384
	ds_read_b128 v[212:215], v99 offset:32768
	ds_read_b128 v[216:219], v99 offset:49152
	v_mfma_f32_16x16x32_f16 v[172:175], v[94:97], v[156:159], v[172:175]
	v_mfma_f32_16x16x32_f16 v[94:97], v[94:97], v[160:163], v[10:13]
	s_nop 2
	v_lshl_add_u64 v[10:11], s[8:9], 4, v[130:131]
	v_mfma_f32_16x16x32_f16 v[180:183], v[90:93], v[156:159], v[180:183]
	v_mfma_f32_16x16x32_f16 v[90:93], v[90:93], v[160:163], v[18:21]
	v_mfma_f32_16x16x32_f16 v[188:191], v[78:81], v[156:159], v[188:191]
	v_mfma_f32_16x16x32_f16 v[78:81], v[78:81], v[160:163], v[22:25]
	global_load_dwordx4 v[30:33], v[10:11], off
	s_nop 1
	global_load_dwordx4 v[22:25], v[10:11], off offset:1024
	global_load_dwordx4 v[18:21], v[10:11], off offset:2048
	s_nop 0
	global_load_dwordx4 v[10:13], v[10:11], off offset:3072
	s_nop 0
	global_load_dwordx2 v[134:135], v[0:1], off
	v_mfma_f32_16x16x32_f16 v[126:129], v[34:37], v[156:159], v[126:129]
	v_mfma_f32_16x16x32_f16 v[34:37], v[34:37], v[160:163], v[38:41]
	s_nop 2
	v_add_u32_e32 v100, s67, v100
	ds_read_b128 v[38:41], v100
	ds_read_b128 v[156:159], v100 offset:16384
	ds_read_b128 v[160:163], v100 offset:32768
	ds_read_b128 v[228:231], v100 offset:49152
	s_add_i32 s8, s22, s36
	s_waitcnt vmcnt(20) lgkmcnt(7)
	v_mfma_f32_16x16x32_f16 v[164:167], v[82:85], v[136:139], v[164:167]
	s_waitcnt lgkmcnt(6)
	v_mfma_f32_16x16x32_f16 v[168:171], v[82:85], v[208:211], v[168:171]
	s_waitcnt lgkmcnt(5)
	v_mfma_f32_16x16x32_f16 v[172:175], v[82:85], v[212:215], v[172:175]
	s_waitcnt lgkmcnt(4)
	v_mfma_f32_16x16x32_f16 v[82:85], v[82:85], v[216:219], v[94:97]
	s_waitcnt vmcnt(19)
	v_mfma_f32_16x16x32_f16 v[58:61], v[70:73], v[136:139], v[58:61]
	v_mfma_f32_16x16x32_f16 v[94:97], v[70:73], v[208:211], v[176:179]
	v_mfma_f32_16x16x32_f16 v[176:179], v[70:73], v[212:215], v[180:183]
	v_mfma_f32_16x16x32_f16 v[70:73], v[70:73], v[216:219], v[90:93]
	s_waitcnt vmcnt(18)
	v_mfma_f32_16x16x32_f16 v[54:57], v[62:65], v[136:139], v[54:57]
	v_mfma_f32_16x16x32_f16 v[90:93], v[62:65], v[208:211], v[184:187]
	v_mfma_f32_16x16x32_f16 v[180:183], v[62:65], v[212:215], v[188:191]
	v_mfma_f32_16x16x32_f16 v[62:65], v[62:65], v[216:219], v[78:81]
	s_waitcnt vmcnt(17)
	v_mfma_f32_16x16x32_f16 v[50:53], v[42:45], v[136:139], v[50:53]
	v_mfma_f32_16x16x32_f16 v[78:81], v[42:45], v[208:211], v[122:125]
	v_mfma_f32_16x16x32_f16 v[122:125], v[42:45], v[212:215], v[126:129]
	s_nop 2
	buffer_load_dwordx4 v[126:129], v147, s[16:19], s8 offen
	buffer_load_dwordx4 v[136:139], v148, s[16:19], s8 offen
	buffer_load_dwordx4 v[184:187], v149, s[16:19], s8 offen
	buffer_load_dwordx4 v[188:191], v150, s[16:19], s8 offen
	v_mfma_f32_16x16x32_f16 v[34:37], v[42:45], v[216:219], v[34:37]
	v_add_u32_e32 v111, s68, v111
	ds_read_b128 v[42:45], v111
	ds_read_b128 v[208:211], v111 offset:16384
	ds_read_b128 v[212:215], v111 offset:32768
	ds_read_b128 v[216:219], v111 offset:49152
	s_add_i32 s8, s22, s37
	s_waitcnt vmcnt(20) lgkmcnt(7)
	v_mfma_f32_16x16x32_f16 v[164:167], v[86:89], v[38:41], v[164:167]
	s_waitcnt lgkmcnt(6)
	v_mfma_f32_16x16x32_f16 v[168:171], v[86:89], v[156:159], v[168:171]
	s_waitcnt lgkmcnt(5)
	v_mfma_f32_16x16x32_f16 v[172:175], v[86:89], v[160:163], v[172:175]
	s_waitcnt lgkmcnt(4)
	v_mfma_f32_16x16x32_f16 v[82:85], v[86:89], v[228:231], v[82:85]
	s_waitcnt vmcnt(19)
	v_mfma_f32_16x16x32_f16 v[58:61], v[74:77], v[38:41], v[58:61]
	v_mfma_f32_16x16x32_f16 v[86:89], v[74:77], v[156:159], v[94:97]
	v_mfma_f32_16x16x32_f16 v[94:97], v[74:77], v[160:163], v[176:179]
	v_mfma_f32_16x16x32_f16 v[70:73], v[74:77], v[228:231], v[70:73]
	s_waitcnt vmcnt(18)
	v_mfma_f32_16x16x32_f16 v[54:57], v[66:69], v[38:41], v[54:57]
	v_mfma_f32_16x16x32_f16 v[74:77], v[66:69], v[156:159], v[90:93]
	v_mfma_f32_16x16x32_f16 v[90:93], v[66:69], v[160:163], v[180:183]
	v_mfma_f32_16x16x32_f16 v[62:65], v[66:69], v[228:231], v[62:65]
	s_waitcnt vmcnt(17)
	v_mfma_f32_16x16x32_f16 v[38:41], v[46:49], v[38:41], v[50:53]
	v_mfma_f32_16x16x32_f16 v[50:53], v[46:49], v[156:159], v[78:81]
	v_mfma_f32_16x16x32_f16 v[66:69], v[46:49], v[160:163], v[122:125]
	s_nop 1
	buffer_load_dwordx4 v[78:81], v147, s[16:19], s8 offen
	buffer_load_dwordx4 v[122:125], v148, s[16:19], s8 offen
	buffer_load_dwordx4 v[156:159], v149, s[16:19], s8 offen
	buffer_load_dwordx4 v[160:163], v150, s[16:19], s8 offen
	v_mfma_f32_16x16x32_f16 v[34:37], v[46:49], v[228:231], v[34:37]
	v_add_u32_e32 v98, s69, v98
	ds_read_b128 v[46:49], v98
	ds_read_b128 v[176:179], v98 offset:16384
	ds_read_b128 v[180:183], v98 offset:32768
	ds_read_b128 v[228:231], v98 offset:49152
	s_add_i32 s8, s22, s38
	s_waitcnt vmcnt(20) lgkmcnt(7)
	v_mfma_f32_16x16x32_f16 v[164:167], v[192:195], v[42:45], v[164:167]
	s_waitcnt lgkmcnt(6)
	v_mfma_f32_16x16x32_f16 v[168:171], v[192:195], v[208:211], v[168:171]
	s_waitcnt lgkmcnt(5)
	v_mfma_f32_16x16x32_f16 v[172:175], v[192:195], v[212:215], v[172:175]
	s_waitcnt lgkmcnt(4)
	v_mfma_f32_16x16x32_f16 v[82:85], v[192:195], v[216:219], v[82:85]
	s_waitcnt vmcnt(19)
	v_mfma_f32_16x16x32_f16 v[58:61], v[196:199], v[42:45], v[58:61]
	v_mfma_f32_16x16x32_f16 v[86:89], v[196:199], v[208:211], v[86:89]
	v_mfma_f32_16x16x32_f16 v[94:97], v[196:199], v[212:215], v[94:97]
	v_mfma_f32_16x16x32_f16 v[70:73], v[196:199], v[216:219], v[70:73]
	s_waitcnt vmcnt(18)
	v_mfma_f32_16x16x32_f16 v[54:57], v[200:203], v[42:45], v[54:57]
	v_mfma_f32_16x16x32_f16 v[74:77], v[200:203], v[208:211], v[74:77]
	v_mfma_f32_16x16x32_f16 v[90:93], v[200:203], v[212:215], v[90:93]
	v_mfma_f32_16x16x32_f16 v[62:65], v[200:203], v[216:219], v[62:65]
	s_waitcnt vmcnt(17)
	v_mfma_f32_16x16x32_f16 v[38:41], v[204:207], v[42:45], v[38:41]
	v_mfma_f32_16x16x32_f16 v[42:45], v[204:207], v[208:211], v[50:53]
	v_mfma_f32_16x16x32_f16 v[50:53], v[204:207], v[212:215], v[66:69]
	s_nop 2
	buffer_load_dwordx4 v[66:69], v147, s[16:19], s8 offen
	buffer_load_dwordx4 v[192:195], v148, s[16:19], s8 offen
	buffer_load_dwordx4 v[196:199], v149, s[16:19], s8 offen
	buffer_load_dwordx4 v[200:203], v150, s[16:19], s8 offen
	v_mfma_f32_16x16x32_f16 v[34:37], v[204:207], v[216:219], v[34:37]
	v_add_u32_e32 v99, s70, v99
	ds_read_b128 v[204:207], v99
	ds_read_b128 v[208:211], v99 offset:16384
	ds_read_b128 v[212:215], v99 offset:32768
	ds_read_b128 v[216:219], v99 offset:49152
	s_add_i32 s8, s22, s39
	s_waitcnt vmcnt(20) lgkmcnt(7)
	v_mfma_f32_16x16x32_f16 v[164:167], v[140:143], v[46:49], v[164:167]
	s_waitcnt lgkmcnt(6)
	v_mfma_f32_16x16x32_f16 v[168:171], v[140:143], v[176:179], v[168:171]
	s_waitcnt lgkmcnt(5)
	v_mfma_f32_16x16x32_f16 v[172:175], v[140:143], v[180:183], v[172:175]
	s_waitcnt lgkmcnt(4)
	v_mfma_f32_16x16x32_f16 v[82:85], v[140:143], v[228:231], v[82:85]
	s_waitcnt vmcnt(19)
	v_mfma_f32_16x16x32_f16 v[58:61], v[220:223], v[46:49], v[58:61]
	v_mfma_f32_16x16x32_f16 v[86:89], v[220:223], v[176:179], v[86:89]
	s_waitcnt vmcnt(18)
	v_mfma_f32_16x16x32_f16 v[54:57], v[152:155], v[46:49], v[54:57]
	v_mfma_f32_16x16x32_f16 v[74:77], v[152:155], v[176:179], v[74:77]
	v_mfma_f32_16x16x32_f16 v[90:93], v[152:155], v[180:183], v[90:93]
	v_mfma_f32_16x16x32_f16 v[62:65], v[152:155], v[228:231], v[62:65]
	s_waitcnt vmcnt(17)
	v_mfma_f32_16x16x32_f16 v[38:41], v[224:227], v[46:49], v[38:41]
	v_mfma_f32_16x16x32_f16 v[42:45], v[224:227], v[176:179], v[42:45]
	v_mfma_f32_16x16x32_f16 v[46:49], v[224:227], v[180:183], v[50:53]
	s_nop 2
	buffer_load_dwordx4 v[50:53], v147, s[16:19], s8 offen
	buffer_load_dwordx4 v[140:143], v148, s[16:19], s8 offen
	buffer_load_dwordx4 v[152:155], v149, s[16:19], s8 offen
	buffer_load_dwordx4 v[176:179], v150, s[16:19], s8 offen
	v_mfma_f32_16x16x32_f16 v[94:97], v[220:223], v[180:183], v[94:97]
	v_mfma_f32_16x16x32_f16 v[70:73], v[220:223], v[228:231], v[70:73]
	v_mfma_f32_16x16x32_f16 v[34:37], v[224:227], v[228:231], v[34:37]
	v_add_u32_e32 v100, s71, v100
	ds_read_b128 v[180:183], v100
	ds_read_b128 v[220:223], v100 offset:16384
	ds_read_b128 v[224:227], v100 offset:32768
	ds_read_b128 v[228:231], v100 offset:49152
	s_add_i32 s8, s22, s40
	s_waitcnt vmcnt(15) lgkmcnt(7)
	v_mfma_f32_16x16x32_f16 v[164:167], v[126:129], v[204:207], v[164:167]
	s_waitcnt lgkmcnt(6)
	v_mfma_f32_16x16x32_f16 v[168:171], v[126:129], v[208:211], v[168:171]
	s_waitcnt lgkmcnt(5)
	v_mfma_f32_16x16x32_f16 v[172:175], v[126:129], v[212:215], v[172:175]
	s_waitcnt lgkmcnt(4)
	v_mfma_f32_16x16x32_f16 v[82:85], v[126:129], v[216:219], v[82:85]
	s_waitcnt vmcnt(14)
	v_mfma_f32_16x16x32_f16 v[58:61], v[136:139], v[204:207], v[58:61]
	v_mfma_f32_16x16x32_f16 v[86:89], v[136:139], v[208:211], v[86:89]
	v_mfma_f32_16x16x32_f16 v[94:97], v[136:139], v[212:215], v[94:97]
	v_mfma_f32_16x16x32_f16 v[70:73], v[136:139], v[216:219], v[70:73]
	s_waitcnt vmcnt(13)
	v_mfma_f32_16x16x32_f16 v[54:57], v[184:187], v[204:207], v[54:57]
	v_mfma_f32_16x16x32_f16 v[74:77], v[184:187], v[208:211], v[74:77]
	v_mfma_f32_16x16x32_f16 v[90:93], v[184:187], v[212:215], v[90:93]
	v_mfma_f32_16x16x32_f16 v[62:65], v[184:187], v[216:219], v[62:65]
	s_waitcnt vmcnt(12)
	v_mfma_f32_16x16x32_f16 v[38:41], v[188:191], v[204:207], v[38:41]
	buffer_load_dwordx4 v[126:129], v147, s[16:19], s8 offen
	buffer_load_dwordx4 v[136:139], v148, s[16:19], s8 offen
	buffer_load_dwordx4 v[184:187], v149, s[16:19], s8 offen
	buffer_load_dwordx4 v[204:207], v150, s[16:19], s8 offen
	v_mfma_f32_16x16x32_f16 v[42:45], v[188:191], v[208:211], v[42:45]
	v_mfma_f32_16x16x32_f16 v[46:49], v[188:191], v[212:215], v[46:49]
	v_mfma_f32_16x16x32_f16 v[34:37], v[188:191], v[216:219], v[34:37]
	v_add_u32_e32 v111, s72, v111
	ds_read_b128 v[188:191], v111
	ds_read_b128 v[208:211], v111 offset:16384
	ds_read_b128 v[212:215], v111 offset:32768
	ds_read_b128 v[216:219], v111 offset:49152
	s_add_i32 s8, s22, s41
	s_waitcnt vmcnt(15) lgkmcnt(7)
	v_mfma_f32_16x16x32_f16 v[164:167], v[78:81], v[180:183], v[164:167]
	s_waitcnt lgkmcnt(6)
	v_mfma_f32_16x16x32_f16 v[168:171], v[78:81], v[220:223], v[168:171]
	s_waitcnt lgkmcnt(5)
	v_mfma_f32_16x16x32_f16 v[172:175], v[78:81], v[224:227], v[172:175]
	s_waitcnt lgkmcnt(4)
	v_mfma_f32_16x16x32_f16 v[78:81], v[78:81], v[228:231], v[82:85]
	s_waitcnt vmcnt(14)
	v_mfma_f32_16x16x32_f16 v[58:61], v[122:125], v[180:183], v[58:61]
	v_mfma_f32_16x16x32_f16 v[82:85], v[122:125], v[220:223], v[86:89]
	v_mfma_f32_16x16x32_f16 v[86:89], v[122:125], v[224:227], v[94:97]
	v_mfma_f32_16x16x32_f16 v[70:73], v[122:125], v[228:231], v[70:73]
	s_waitcnt vmcnt(13)
	v_mfma_f32_16x16x32_f16 v[54:57], v[156:159], v[180:183], v[54:57]
	v_mfma_f32_16x16x32_f16 v[74:77], v[156:159], v[220:223], v[74:77]
	v_mfma_f32_16x16x32_f16 v[90:93], v[156:159], v[224:227], v[90:93]
	v_mfma_f32_16x16x32_f16 v[62:65], v[156:159], v[228:231], v[62:65]
	s_waitcnt vmcnt(12)
	v_mfma_f32_16x16x32_f16 v[38:41], v[160:163], v[180:183], v[38:41]
	buffer_load_dwordx4 v[94:97], v147, s[16:19], s8 offen
	buffer_load_dwordx4 v[122:125], v148, s[16:19], s8 offen
	buffer_load_dwordx4 v[156:159], v149, s[16:19], s8 offen
	buffer_load_dwordx4 v[180:183], v150, s[16:19], s8 offen
	v_mfma_f32_16x16x32_f16 v[42:45], v[160:163], v[220:223], v[42:45]
	v_mfma_f32_16x16x32_f16 v[46:49], v[160:163], v[224:227], v[46:49]
	v_mfma_f32_16x16x32_f16 v[34:37], v[160:163], v[228:231], v[34:37]
	v_add_u32_e32 v98, s73, v98
	ds_read_b128 v[160:163], v98
	ds_read_b128 v[220:223], v98 offset:16384
	ds_read_b128 v[224:227], v98 offset:32768
	ds_read_b128 v[228:231], v98 offset:49152
	s_add_i32 s8, s22, s42
	s_waitcnt vmcnt(15) lgkmcnt(7)
	v_mfma_f32_16x16x32_f16 v[164:167], v[66:69], v[188:191], v[164:167]
	s_waitcnt lgkmcnt(6)
	v_mfma_f32_16x16x32_f16 v[168:171], v[66:69], v[208:211], v[168:171]
	s_waitcnt lgkmcnt(5)
	v_mfma_f32_16x16x32_f16 v[172:175], v[66:69], v[212:215], v[172:175]
	s_waitcnt lgkmcnt(4)
	v_mfma_f32_16x16x32_f16 v[66:69], v[66:69], v[216:219], v[78:81]
	s_waitcnt vmcnt(14)
	v_mfma_f32_16x16x32_f16 v[58:61], v[192:195], v[188:191], v[58:61]
	v_mfma_f32_16x16x32_f16 v[78:81], v[192:195], v[208:211], v[82:85]
	v_mfma_f32_16x16x32_f16 v[82:85], v[192:195], v[212:215], v[86:89]
	v_mfma_f32_16x16x32_f16 v[70:73], v[192:195], v[216:219], v[70:73]
	s_waitcnt vmcnt(13)
	v_mfma_f32_16x16x32_f16 v[54:57], v[196:199], v[188:191], v[54:57]
	v_mfma_f32_16x16x32_f16 v[74:77], v[196:199], v[208:211], v[74:77]
	v_mfma_f32_16x16x32_f16 v[86:89], v[196:199], v[212:215], v[90:93]
	v_mfma_f32_16x16x32_f16 v[62:65], v[196:199], v[216:219], v[62:65]
	s_waitcnt vmcnt(12)
	v_mfma_f32_16x16x32_f16 v[38:41], v[200:203], v[188:191], v[38:41]
	buffer_load_dwordx4 v[90:93], v147, s[16:19], s8 offen
	buffer_load_dwordx4 v[188:191], v148, s[16:19], s8 offen
	buffer_load_dwordx4 v[192:195], v149, s[16:19], s8 offen
	buffer_load_dwordx4 v[196:199], v150, s[16:19], s8 offen
	v_mfma_f32_16x16x32_f16 v[42:45], v[200:203], v[208:211], v[42:45]
	v_mfma_f32_16x16x32_f16 v[46:49], v[200:203], v[212:215], v[46:49]
	v_mfma_f32_16x16x32_f16 v[34:37], v[200:203], v[216:219], v[34:37]
	v_add_u32_e32 v99, s74, v99
	ds_read_b128 v[200:203], v99
	ds_read_b128 v[208:211], v99 offset:16384
	ds_read_b128 v[212:215], v99 offset:32768
	ds_read_b128 v[216:219], v99 offset:49152
	s_add_i32 s8, s22, s43
	s_waitcnt vmcnt(15) lgkmcnt(7)
	v_mfma_f32_16x16x32_f16 v[164:167], v[50:53], v[160:163], v[164:167]
	s_waitcnt lgkmcnt(6)
	v_mfma_f32_16x16x32_f16 v[168:171], v[50:53], v[220:223], v[168:171]
	s_waitcnt lgkmcnt(5)
	v_mfma_f32_16x16x32_f16 v[172:175], v[50:53], v[224:227], v[172:175]
	s_waitcnt lgkmcnt(4)
	v_mfma_f32_16x16x32_f16 v[50:53], v[50:53], v[228:231], v[66:69]
	s_waitcnt vmcnt(14)
	v_mfma_f32_16x16x32_f16 v[58:61], v[140:143], v[160:163], v[58:61]
	v_mfma_f32_16x16x32_f16 v[66:69], v[140:143], v[220:223], v[78:81]
	v_mfma_f32_16x16x32_f16 v[78:81], v[140:143], v[224:227], v[82:85]
	v_mfma_f32_16x16x32_f16 v[70:73], v[140:143], v[228:231], v[70:73]
	s_waitcnt vmcnt(13)
	v_mfma_f32_16x16x32_f16 v[54:57], v[152:155], v[160:163], v[54:57]
	v_mfma_f32_16x16x32_f16 v[74:77], v[152:155], v[220:223], v[74:77]
	v_mfma_f32_16x16x32_f16 v[82:85], v[152:155], v[224:227], v[86:89]
	v_mfma_f32_16x16x32_f16 v[62:65], v[152:155], v[228:231], v[62:65]
	s_waitcnt vmcnt(12)
	v_mfma_f32_16x16x32_f16 v[38:41], v[176:179], v[160:163], v[38:41]
	buffer_load_dwordx4 v[86:89], v147, s[16:19], s8 offen
	buffer_load_dwordx4 v[140:143], v148, s[16:19], s8 offen
	buffer_load_dwordx4 v[152:155], v149, s[16:19], s8 offen
	buffer_load_dwordx4 v[160:163], v150, s[16:19], s8 offen
	v_mfma_f32_16x16x32_f16 v[42:45], v[176:179], v[220:223], v[42:45]
	v_mfma_f32_16x16x32_f16 v[46:49], v[176:179], v[224:227], v[46:49]
	v_mfma_f32_16x16x32_f16 v[34:37], v[176:179], v[228:231], v[34:37]
	v_add_u32_e32 v100, s75, v100
	ds_read_b128 v[176:179], v100
	ds_read_b128 v[220:223], v100 offset:16384
	ds_read_b128 v[224:227], v100 offset:32768
	ds_read_b128 v[228:231], v100 offset:49152
	s_add_i32 s8, s22, s44
	s_waitcnt vmcnt(15) lgkmcnt(7)
	v_mfma_f32_16x16x32_f16 v[164:167], v[126:129], v[200:203], v[164:167]
	s_waitcnt lgkmcnt(6)
	v_mfma_f32_16x16x32_f16 v[168:171], v[126:129], v[208:211], v[168:171]
	s_waitcnt lgkmcnt(5)
	v_mfma_f32_16x16x32_f16 v[172:175], v[126:129], v[212:215], v[172:175]
	s_waitcnt lgkmcnt(4)
	v_mfma_f32_16x16x32_f16 v[50:53], v[126:129], v[216:219], v[50:53]
	s_waitcnt vmcnt(14)
	v_mfma_f32_16x16x32_f16 v[58:61], v[136:139], v[200:203], v[58:61]
	v_mfma_f32_16x16x32_f16 v[66:69], v[136:139], v[208:211], v[66:69]
	v_mfma_f32_16x16x32_f16 v[78:81], v[136:139], v[212:215], v[78:81]
	v_mfma_f32_16x16x32_f16 v[70:73], v[136:139], v[216:219], v[70:73]
	s_waitcnt vmcnt(13)
	v_mfma_f32_16x16x32_f16 v[54:57], v[184:187], v[200:203], v[54:57]
	v_mfma_f32_16x16x32_f16 v[74:77], v[184:187], v[208:211], v[74:77]
	v_mfma_f32_16x16x32_f16 v[82:85], v[184:187], v[212:215], v[82:85]
	v_mfma_f32_16x16x32_f16 v[62:65], v[184:187], v[216:219], v[62:65]
	s_waitcnt vmcnt(12)
	v_mfma_f32_16x16x32_f16 v[38:41], v[204:207], v[200:203], v[38:41]
	buffer_load_dwordx4 v[126:129], v147, s[16:19], s8 offen
	buffer_load_dwordx4 v[136:139], v148, s[16:19], s8 offen
	buffer_load_dwordx4 v[184:187], v149, s[16:19], s8 offen
	buffer_load_dwordx4 v[200:203], v150, s[16:19], s8 offen
	v_mfma_f32_16x16x32_f16 v[42:45], v[204:207], v[208:211], v[42:45]
	v_mfma_f32_16x16x32_f16 v[46:49], v[204:207], v[212:215], v[46:49]
	v_mfma_f32_16x16x32_f16 v[34:37], v[204:207], v[216:219], v[34:37]
	v_add_u32_e32 v111, s76, v111
	ds_read_b128 v[204:207], v111
	ds_read_b128 v[208:211], v111 offset:16384
	ds_read_b128 v[212:215], v111 offset:32768
	ds_read_b128 v[216:219], v111 offset:49152
	s_add_i32 s8, s22, s45
	s_waitcnt vmcnt(15) lgkmcnt(7)
	v_mfma_f32_16x16x32_f16 v[164:167], v[94:97], v[176:179], v[164:167]
	s_waitcnt lgkmcnt(6)
	v_mfma_f32_16x16x32_f16 v[168:171], v[94:97], v[220:223], v[168:171]
	s_waitcnt vmcnt(14)
	v_mfma_f32_16x16x32_f16 v[58:61], v[122:125], v[176:179], v[58:61]
	v_mfma_f32_16x16x32_f16 v[66:69], v[122:125], v[220:223], v[66:69]
	s_waitcnt lgkmcnt(5)
	v_mfma_f32_16x16x32_f16 v[78:81], v[122:125], v[224:227], v[78:81]
	s_waitcnt lgkmcnt(4)
	v_mfma_f32_16x16x32_f16 v[70:73], v[122:125], v[228:231], v[70:73]
	s_waitcnt vmcnt(13)
	v_mfma_f32_16x16x32_f16 v[54:57], v[156:159], v[176:179], v[54:57]
	v_mfma_f32_16x16x32_f16 v[74:77], v[156:159], v[220:223], v[74:77]
	v_mfma_f32_16x16x32_f16 v[82:85], v[156:159], v[224:227], v[82:85]
	v_mfma_f32_16x16x32_f16 v[62:65], v[156:159], v[228:231], v[62:65]
	s_waitcnt vmcnt(12)
	v_mfma_f32_16x16x32_f16 v[38:41], v[180:183], v[176:179], v[38:41]
	v_mfma_f32_16x16x32_f16 v[42:45], v[180:183], v[220:223], v[42:45]
	buffer_load_dwordx4 v[122:125], v147, s[16:19], s8 offen
	buffer_load_dwordx4 v[156:159], v148, s[16:19], s8 offen
	buffer_load_dwordx4 v[176:179], v149, s[16:19], s8 offen
	buffer_load_dwordx4 v[220:223], v150, s[16:19], s8 offen
	v_mfma_f32_16x16x32_f16 v[50:53], v[94:97], v[228:231], v[50:53]
	v_mfma_f32_16x16x32_f16 v[46:49], v[180:183], v[224:227], v[46:49]
	v_mfma_f32_16x16x32_f16 v[34:37], v[180:183], v[228:231], v[34:37]
	v_mfma_f32_16x16x32_f16 v[172:175], v[94:97], v[224:227], v[172:175]
	v_add_u32_e32 v98, s77, v98
	ds_read_b128 v[94:97], v98
	ds_read_b128 v[180:183], v98 offset:16384
	ds_read_b128 v[224:227], v98 offset:32768
	ds_read_b128 v[228:231], v98 offset:49152
	s_add_i32 s8, s22, s46
	s_waitcnt vmcnt(15) lgkmcnt(7)
	v_mfma_f32_16x16x32_f16 v[164:167], v[90:93], v[204:207], v[164:167]
	s_waitcnt lgkmcnt(6)
	v_mfma_f32_16x16x32_f16 v[168:171], v[90:93], v[208:211], v[168:171]
	s_waitcnt lgkmcnt(5)
	v_mfma_f32_16x16x32_f16 v[172:175], v[90:93], v[212:215], v[172:175]
	s_waitcnt lgkmcnt(4)
	v_mfma_f32_16x16x32_f16 v[90:93], v[90:93], v[216:219], v[50:53]
	s_waitcnt vmcnt(14)
	v_mfma_f32_16x16x32_f16 v[232:235], v[188:191], v[204:207], v[58:61]
	v_mfma_f32_16x16x32_f16 v[66:69], v[188:191], v[208:211], v[66:69]
	v_mfma_f32_16x16x32_f16 v[78:81], v[188:191], v[212:215], v[78:81]
	v_mfma_f32_16x16x32_f16 v[70:73], v[188:191], v[216:219], v[70:73]
	s_waitcnt vmcnt(13)
	v_mfma_f32_16x16x32_f16 v[188:191], v[192:195], v[204:207], v[54:57]
	v_mfma_f32_16x16x32_f16 v[74:77], v[192:195], v[208:211], v[74:77]
	v_mfma_f32_16x16x32_f16 v[82:85], v[192:195], v[212:215], v[82:85]
	v_mfma_f32_16x16x32_f16 v[62:65], v[192:195], v[216:219], v[62:65]
	s_waitcnt vmcnt(12)
	v_mfma_f32_16x16x32_f16 v[192:195], v[196:199], v[204:207], v[38:41]
	buffer_load_dwordx4 v[58:61], v147, s[16:19], s8 offen
	buffer_load_dwordx4 v[54:57], v148, s[16:19], s8 offen
	buffer_load_dwordx4 v[50:53], v149, s[16:19], s8 offen
	buffer_load_dwordx4 v[38:41], v150, s[16:19], s8 offen
	v_mfma_f32_16x16x32_f16 v[42:45], v[196:199], v[208:211], v[42:45]
	v_mfma_f32_16x16x32_f16 v[46:49], v[196:199], v[212:215], v[46:49]
	v_mfma_f32_16x16x32_f16 v[196:199], v[196:199], v[216:219], v[34:37]
	v_add_u32_e32 v99, s78, v99
	ds_read_b128 v[204:207], v99
	ds_read_b128 v[208:211], v99 offset:16384
	ds_read_b128 v[212:215], v99 offset:32768
	ds_read_b128 v[216:219], v99 offset:49152
	s_add_i32 s8, s22, s47
	s_waitcnt vmcnt(15) lgkmcnt(7)
	v_mfma_f32_16x16x32_f16 v[164:167], v[86:89], v[94:97], v[164:167]
	s_waitcnt lgkmcnt(6)
	v_mfma_f32_16x16x32_f16 v[168:171], v[86:89], v[180:183], v[168:171]
	s_waitcnt lgkmcnt(5)
	v_mfma_f32_16x16x32_f16 v[172:175], v[86:89], v[224:227], v[172:175]
	s_waitcnt lgkmcnt(4)
	v_mfma_f32_16x16x32_f16 v[86:89], v[86:89], v[228:231], v[90:93]
	s_waitcnt vmcnt(14)
	v_mfma_f32_16x16x32_f16 v[232:235], v[140:143], v[94:97], v[232:235]
	v_mfma_f32_16x16x32_f16 v[66:69], v[140:143], v[180:183], v[66:69]
	v_mfma_f32_16x16x32_f16 v[236:239], v[140:143], v[224:227], v[78:81]
	v_mfma_f32_16x16x32_f16 v[70:73], v[140:143], v[228:231], v[70:73]
	s_waitcnt vmcnt(13)
	v_mfma_f32_16x16x32_f16 v[140:143], v[152:155], v[94:97], v[188:191]
	v_mfma_f32_16x16x32_f16 v[74:77], v[152:155], v[180:183], v[74:77]
	v_mfma_f32_16x16x32_f16 v[82:85], v[152:155], v[224:227], v[82:85]
	v_mfma_f32_16x16x32_f16 v[62:65], v[152:155], v[228:231], v[62:65]
	s_waitcnt vmcnt(12)
	v_mfma_f32_16x16x32_f16 v[152:155], v[160:163], v[94:97], v[192:195]
	buffer_load_dwordx4 v[94:97], v147, s[16:19], s8 offen
	buffer_load_dwordx4 v[90:93], v148, s[16:19], s8 offen
	buffer_load_dwordx4 v[78:81], v149, s[16:19], s8 offen
	buffer_load_dwordx4 v[34:37], v150, s[16:19], s8 offen
	v_mfma_f32_16x16x32_f16 v[42:45], v[160:163], v[180:183], v[42:45]
	v_mfma_f32_16x16x32_f16 v[46:49], v[160:163], v[224:227], v[46:49]
	v_mfma_f32_16x16x32_f16 v[160:163], v[160:163], v[228:231], v[196:199]
	v_add_u32_e32 v100, s79, v100
	ds_read_b128 v[180:183], v100
	ds_read_b128 v[188:191], v100 offset:16384
	ds_read_b128 v[192:195], v100 offset:32768
	ds_read_b128 v[196:199], v100 offset:49152
	s_add_i32 s8, s22, s48
	s_waitcnt vmcnt(15) lgkmcnt(7)
	v_mfma_f32_16x16x32_f16 v[164:167], v[126:129], v[204:207], v[164:167]
	s_waitcnt lgkmcnt(6)
	v_mfma_f32_16x16x32_f16 v[168:171], v[126:129], v[208:211], v[168:171]
	s_waitcnt lgkmcnt(5)
	v_mfma_f32_16x16x32_f16 v[172:175], v[126:129], v[212:215], v[172:175]
	s_waitcnt lgkmcnt(4)
	v_mfma_f32_16x16x32_f16 v[86:89], v[126:129], v[216:219], v[86:89]
	s_waitcnt vmcnt(14)
	v_mfma_f32_16x16x32_f16 v[126:129], v[136:139], v[204:207], v[232:235]
	v_mfma_f32_16x16x32_f16 v[66:69], v[136:139], v[208:211], v[66:69]
	v_mfma_f32_16x16x32_f16 v[224:227], v[136:139], v[212:215], v[236:239]
	v_mfma_f32_16x16x32_f16 v[136:139], v[136:139], v[216:219], v[70:73]
	s_waitcnt vmcnt(13)
	v_mfma_f32_16x16x32_f16 v[140:143], v[184:187], v[204:207], v[140:143]
	v_mfma_f32_16x16x32_f16 v[74:77], v[184:187], v[208:211], v[74:77]
	v_mfma_f32_16x16x32_f16 v[228:231], v[184:187], v[212:215], v[82:85]
	v_mfma_f32_16x16x32_f16 v[184:187], v[184:187], v[216:219], v[62:65]
	s_waitcnt vmcnt(12)
	v_mfma_f32_16x16x32_f16 v[152:155], v[200:203], v[204:207], v[152:155]
	v_mfma_f32_16x16x32_f16 v[204:207], v[200:203], v[208:211], v[42:45]
	buffer_load_dwordx4 v[82:85], v147, s[16:19], s8 offen
	buffer_load_dwordx4 v[70:73], v148, s[16:19], s8 offen
	buffer_load_dwordx4 v[62:65], v149, s[16:19], s8 offen
	buffer_load_dwordx4 v[42:45], v150, s[16:19], s8 offen
	v_mfma_f32_16x16x32_f16 v[46:49], v[200:203], v[212:215], v[46:49]
	v_mfma_f32_16x16x32_f16 v[160:163], v[200:203], v[216:219], v[160:163]
	v_add_u32_e32 v0, 0x1ac00, v104
	ds_read_b128 v[240:243], v0
	ds_read_b128 v[244:247], v0 offset:16
	s_waitcnt vmcnt(12) lgkmcnt(5)
	v_mfma_f32_16x16x32_f16 v[164:167], v[122:125], v[180:183], v[164:167]
	v_mfma_f32_16x16x32_f16 v[126:129], v[156:159], v[180:183], v[126:129]
	v_mfma_f32_16x16x32_f16 v[140:143], v[176:179], v[180:183], v[140:143]
	v_mfma_f32_16x16x32_f16 v[152:155], v[220:223], v[180:183], v[152:155]
	s_waitcnt lgkmcnt(4)
	v_mfma_f32_16x16x32_f16 v[168:171], v[122:125], v[188:191], v[168:171]
	v_mfma_f32_16x16x32_f16 v[208:211], v[156:159], v[188:191], v[66:69]
	v_mfma_f32_16x16x32_f16 v[212:215], v[176:179], v[188:191], v[74:77]
	v_mfma_f32_16x16x32_f16 v[204:207], v[220:223], v[188:191], v[204:207]
	s_waitcnt lgkmcnt(3)
	v_mfma_f32_16x16x32_f16 v[172:175], v[122:125], v[192:195], v[172:175]
	v_cvt_pk_f16_f32 v232, v164, v165
	v_cvt_pk_f16_f32 v233, v166, v167
	v_pk_max_f16 v232, v232, 0
	v_pk_max_f16 v233, v233, 0
	v_mfma_f32_16x16x32_f16 v[224:227], v[156:159], v[192:195], v[224:227]
	v_cvt_pk_f16_f32 v234, v126, v127
	v_cvt_pk_f16_f32 v235, v128, v129
	v_pk_max_f16 v234, v234, 0
	v_pk_max_f16 v235, v235, 0
	v_mfma_f32_16x16x32_f16 v[228:231], v[176:179], v[192:195], v[228:231]
	v_cvt_pk_f16_f32 v236, v140, v141
	v_cvt_pk_f16_f32 v237, v142, v143
	v_pk_max_f16 v236, v236, 0
	v_pk_max_f16 v237, v237, 0
	v_mfma_f32_16x16x32_f16 v[216:219], v[220:223], v[192:195], v[46:49]
	v_cvt_pk_f16_f32 v238, v152, v153
	v_cvt_pk_f16_f32 v239, v154, v155
	v_pk_max_f16 v238, v238, 0
	v_pk_max_f16 v239, v239, 0
	s_waitcnt lgkmcnt(2)
	v_mfma_f32_16x16x32_f16 v[200:203], v[122:125], v[196:199], v[86:89]
	v_cvt_pk_f16_f32 v180, v168, v169
	v_cvt_pk_f16_f32 v181, v170, v171
	v_pk_max_f16 v180, v180, 0
	v_pk_max_f16 v181, v181, 0
	s_add_i32 s8, s22, s49
	buffer_load_dwordx4 v[86:89], v147, s[16:19], s8 offen
	buffer_load_dwordx4 v[74:77], v148, s[16:19], s8 offen
	buffer_load_dwordx4 v[66:69], v149, s[16:19], s8 offen
	buffer_load_dwordx4 v[46:49], v150, s[16:19], s8 offen
	v_mfma_f32_16x16x32_f16 v[136:139], v[156:159], v[196:199], v[136:139]
	v_cvt_pk_f16_f32 v182, v208, v209
	v_cvt_pk_f16_f32 v183, v210, v211
	v_pk_max_f16 v182, v182, 0
	v_pk_max_f16 v183, v183, 0
	s_waitcnt lgkmcnt(1)
	v_mfma_f32_16x16x32_f16 v[252:255], v[240:243], v[232:235], 0
	v_cvt_pk_f16_f32 v232, v172, v173
	v_cvt_pk_f16_f32 v233, v174, v175
	v_pk_max_f16 v232, v232, 0
	v_pk_max_f16 v233, v233, 0
	v_mfma_f32_16x16x32_f16 v[184:187], v[176:179], v[196:199], v[184:187]
	v_cvt_pk_f16_f32 v188, v212, v213
	v_cvt_pk_f16_f32 v189, v214, v215
	v_pk_max_f16 v188, v188, 0
	v_pk_max_f16 v189, v189, 0
	s_waitcnt lgkmcnt(0)
	v_mfma_f32_16x16x32_f16 v[252:255], v[244:247], v[236:239], v[252:255]
	ds_read_u16 v102, v114
	ds_read_u16 v103, v114 offset:512
	ds_read_u16 v115, v114 offset:1024
	ds_read_u16 v116, v114 offset:1536
	v_cvt_pk_f16_f32 v234, v224, v225
	v_cvt_pk_f16_f32 v235, v226, v227
	v_pk_max_f16 v234, v234, 0
	v_pk_max_f16 v235, v235, 0
	v_mfma_f32_16x16x32_f16 v[160:163], v[220:223], v[196:199], v[160:163]
	v_cvt_pk_f16_f32 v190, v204, v205
	v_cvt_pk_f16_f32 v191, v206, v207
	v_pk_max_f16 v190, v190, 0
	v_pk_max_f16 v191, v191, 0
	v_mfma_f32_16x16x32_f16 v[192:195], v[240:243], v[180:183], 0
	v_cvt_pk_f16_f32 v236, v228, v229
	v_cvt_pk_f16_f32 v237, v230, v231
	v_pk_max_f16 v236, v236, 0
	v_pk_max_f16 v237, v237, 0
	v_mfma_f32_16x16x32_f16 v[192:195], v[244:247], v[188:191], v[192:195]
	v_cvt_pk_f16_f32 v238, v216, v217
	v_cvt_pk_f16_f32 v239, v218, v219
	v_pk_max_f16 v238, v238, 0
	v_pk_max_f16 v239, v239, 0
	v_cvt_pk_f16_f32 v180, v200, v201
	v_cvt_pk_f16_f32 v181, v202, v203
	v_pk_max_f16 v180, v180, 0
	v_pk_max_f16 v181, v181, 0
	v_mfma_f32_16x16x32_f16 v[196:199], v[240:243], v[232:235], 0
	v_cvt_pk_f16_f32 v182, v136, v137
	v_cvt_pk_f16_f32 v183, v138, v139
	v_pk_max_f16 v182, v182, 0
	v_pk_max_f16 v183, v183, 0
	v_mfma_f32_16x16x32_f16 v[196:199], v[244:247], v[236:239], v[196:199]
	v_cvt_pk_f16_f32 v188, v184, v185
	v_cvt_pk_f16_f32 v189, v186, v187
	v_pk_max_f16 v188, v188, 0
	v_pk_max_f16 v189, v189, 0
	v_cvt_pk_f16_f32 v190, v160, v161
	v_cvt_pk_f16_f32 v191, v162, v163
	v_pk_max_f16 v190, v190, 0
	v_pk_max_f16 v191, v191, 0
	v_mfma_f32_16x16x32_f16 v[122:125], v[240:243], v[180:183], 0
	s_nop 0
	v_mfma_f32_16x16x32_f16 v[122:125], v[244:247], v[188:191], v[122:125]
	v_add_u32_e32 v145, 0x12c00, v105
	ds_read_b128 v[240:243], v145 offset:2048
	ds_read_b128 v[244:247], v145 offset:2064
	ds_read_b128 v[248:251], v145 offset:2080
	s_load_dword s30, s[12:13], 0x0
	v_cndmask_b32_e64 v0, v252, v192, s[2:3]
	ds_read_b128 v[252:255], v145 offset:2096
	v_cndmask_b32_e64 v0, v0, v196, s[0:1]
	v_cndmask_b32_e64 v0, v0, v122, s[26:27]
	ds_write_b32 v112, v0
	s_waitcnt vmcnt(16)
	v_cndmask_b32_e64 v1, v30, v134, s[0:1]
	v_bfi_b32 v30, s10, v1, v30
	v_perm_b32 v1, v22, v134, s24
	v_cndmask_b32_e64 v22, v22, v1, s[0:1]
	v_bfi_b32 v1, s10, v135, v18
	v_perm_b32 v121, v10, v135, s24
	v_cndmask_b32_e64 v18, v18, v1, s[0:1]
	v_cndmask_b32_e64 v10, v10, v121, s[0:1]
	s_add_i32 s22, s22, 0x80000
	s_add_i32 s11, s11, 1
	s_add_u32 s12, s12, 4
	s_addc_u32 s13, s13, 0
	v_add_u32_e32 v104, 0x400, v104
	v_add_u32_e32 v105, 0x800, v105
	v_add_u32_e32 v114, 2, v114
	s_cmp_eq_u32 s22, 0x898000
	s_waitcnt lgkmcnt(0)
	s_barrier
	ds_read_b128 v[232:235], v113
	ds_read_b128 v[236:239], v113 offset:1024
	s_waitcnt lgkmcnt(0)
	v_add_f32_e32 v0, v232, v233
	v_add_f32_e32 v1, v234, v235
	v_add_f32_e32 v121, v236, v237
	v_add_f32_e32 v144, v238, v239
	v_add_f32_e32 v0, v0, v1
	v_add_f32_e32 v121, v121, v144
	v_add_f32_e32 v0, v0, v121
	v_add_f32_e32 v0, s30, v0
	ds_write_b32 v106, v0
	v_cvt_f16_f32_e32 v1, v0
	v_cvt_f16_f32_e32 v121, v0
	s_nop 1
	v_permlane16_swap_b32_e32 v1, v121
	v_mov_b32_e32 v144, v1
	v_mov_b32_e32 v145, v121
	s_nop 1
	v_permlane32_swap_b32_e32 v1, v144
	v_permlane32_swap_b32_e32 v121, v145
	v_add_u32_e32 v106, 4, v106
	s_cbranch_scc0 .LBB1_4
